# rope-table frequency f=c^j hoisted out of the per-entry loop in the prologue (computed once per thread, bit-identical), plus v_mov_b64 accumulator zeroing
# speedup vs baseline: 1.0384x; 1.0019x over previous
.LBB0_56:
	s_or_b64 exec, exec, s[8:9]
	s_mov_b32 s0, 0x80000
	v_cmp_gt_i32_e32 vcc, s0, v0
	s_and_saveexec_b64 s[8:9], vcc
	s_cbranch_execz .LBB0_63
	s_add_u32 s10, s78, 0x100000
	s_addc_u32 s11, s79, 0
	s_add_u32 s12, s78, 0x300000
	v_and_b32_e32 v4, 31, v28
	s_mov_b32 s16, 0x24115d99
	s_mov_b32 s18, 0x6dc9c883
	s_addc_u32 s13, s79, 0
	v_cmp_ne_u32_e32 vcc, 0, v4
	s_mov_b64 s[14:15], 0
	s_mov_b32 s17, 0x3fe7ff22
	s_mov_b32 s19, 0x3fc45f30
	s_mov_b32 s5, 0x7ffff
	v_mov_b64_e32 v[14:15], 1.0
	s_and_saveexec_b64 s[20:21], vcc
	s_cbranch_execz .Lrope_f_done
	s_mov_b64 s[22:23], 0
	v_mov_b32_e32 v1, v4
.Lrope_f_loop:
	v_add_u32_e32 v1, -1, v1
	v_cmp_eq_u32_e64 s[0:1], 0, v1
	s_or_b64 s[22:23], s[0:1], s[22:23]
	v_mul_f64 v[14:15], v[14:15], s[16:17]
	s_andn2_b64 exec, exec, s[22:23]
	s_cbranch_execnz .Lrope_f_loop
.Lrope_f_done:
	s_or_b64 exec, exec, s[20:21]
	s_branch .LBB0_58
.LBB0_58:
	v_ashrrev_i32_e32 v6, 5, v0
	v_readlane_b32 s48, v249, 2
	v_ashrrev_i32_e32 v7, 31, v6
	v_readlane_b32 s52, v249, 6
	v_readlane_b32 s53, v249, 7
	v_ashrrev_i32_e32 v1, 31, v0
	v_readlane_b32 s49, v249, 3
	v_lshl_add_u64 v[6:7], v[6:7], 2, s[52:53]
	global_load_dword v5, v[6:7], off
	v_lshlrev_b64 v[6:7], 2, v[0:1]
	v_add_u32_e32 v0, s6, v0
	v_cmp_lt_i32_e64 s[0:1], s5, v0
	v_lshl_add_u64 v[8:9], s[10:11], 0, v[6:7]
	s_or_b64 s[14:15], s[0:1], s[14:15]
	v_readlane_b32 s50, v249, 4
	v_readlane_b32 s51, v249, 5
	v_readlane_b32 s54, v249, 8
	v_readlane_b32 s55, v249, 9
	v_readlane_b32 s56, v249, 10
	v_readlane_b32 s57, v249, 11
	v_readlane_b32 s58, v249, 12
	v_readlane_b32 s59, v249, 13
	v_readlane_b32 s60, v249, 14
	v_readlane_b32 s61, v249, 15
	v_readlane_b32 s62, v249, 16
	v_readlane_b32 s63, v249, 17
	v_lshl_add_u64 v[6:7], s[12:13], 0, v[6:7]
	s_waitcnt vmcnt(0)
	v_cvt_f64_i32_e32 v[10:11], v5
	v_mul_f64 v[2:3], v[14:15], v[10:11]
	v_mul_f64 v[10:11], v[2:3], s[18:19]
	v_floor_f64_e32 v[10:11], v[10:11]
	v_fma_f64 v[2:3], v[2:3], s[18:19], -v[10:11]
	v_cvt_f32_f64_e32 v1, v[2:3]
	v_cos_f32_e32 v2, v1
	v_sin_f32_e32 v1, v1
	global_store_dword v[8:9], v2, off
	global_store_dword v[6:7], v1, off
	s_andn2_b64 exec, exec, s[14:15]
	s_cbranch_execz .LBB0_63
.LBB0_59:
	s_branch .LBB0_58
.LBB0_63:
	s_or_b64 exec, exec, s[8:9]
	s_barrier
	s_getreg_b32 s0, hwreg(HW_REG_HW_ID, 0, 6)
	s_lshl_b32 s0, s0, 2
	s_and_b32 s0, s0, 0xfc
	s_add_i32 s0, s0, 0
	s_add_i32 s0, s0, 0x25c00
	v_mov_b32_e32 v0, s0
	ds_read_b32 v0, v0
	s_waitcnt lgkmcnt(0)
	v_readfirstlane_b32 s0, v0
	v_mbcnt_lo_u32_b32 v0, -1, 0
	v_mbcnt_hi_u32_b32 v0, -1, v0
	s_nop 1
	v_lshl_add_u32 v0, s0, 6, v0
	s_nop 0
	v_cmp_eq_u32_e32 vcc, 0, v0
	s_and_saveexec_b64 s[0:1], vcc
	s_cbranch_execz .LBB0_72
	s_add_u32 s6, s78, 0x8200
	s_addc_u32 s7, s79, 0
	s_mov_b32 s5, 0x400001
	v_mov_b32_e32 v0, 0
	s_movk_i32 s10, 0xbf
	s_movk_i32 s11, 0xc0
	s_branch .LBB0_66

.LBB0_251:
	s_ashr_i32 s25, s24, 31
	s_lshl_b64 s[26:27], s[24:25], 19
	s_add_u32 s5, s90, s26
	s_addc_u32 s18, s91, s27
	s_and_b64 s[26:27], s[28:29], exec
	s_cselect_b32 s26, s5, s30
	s_cselect_b32 s27, s18, s31
	s_ashr_i32 s23, s22, 31
	s_lshl_b64 s[38:39], s[22:23], 19
	s_add_u32 s5, s49, s38
	s_addc_u32 s18, s50, s39
	s_and_b64 s[28:29], s[28:29], exec
	s_cselect_b32 s28, s5, s34
	s_cselect_b32 s29, s18, s35
	s_add_u32 s5, s34, 0x100
	s_addc_u32 s18, s35, 0
	s_add_u32 s30, s30, 0x60080
	v_mov_b32_e32 v0, 0
	s_addc_u32 s31, s31, 0
	s_mov_b32 s23, -2
	v_mov_b64_e32 v[0:1], 0
	v_mov_b64_e32 v[2:3], 0
	v_mov_b64_e32 v[8:9], 0
	v_mov_b64_e32 v[10:11], 0
	v_mov_b64_e32 v[16:17], 0
	v_mov_b64_e32 v[18:19], 0
	v_mov_b64_e32 v[24:25], 0
	v_mov_b64_e32 v[26:27], 0
	v_mov_b64_e32 v[32:33], 0
	v_mov_b64_e32 v[34:35], 0
	v_mov_b64_e32 v[48:49], 0
	v_mov_b64_e32 v[50:51], 0
	v_mov_b64_e32 v[64:65], 0
	v_mov_b64_e32 v[66:67], 0
	v_mov_b64_e32 v[72:73], 0
	v_mov_b64_e32 v[74:75], 0
	v_mov_b64_e32 v[4:5], 0
	v_mov_b64_e32 v[6:7], 0
	v_mov_b64_e32 v[12:13], 0
	v_mov_b64_e32 v[14:15], 0
	v_mov_b64_e32 v[20:21], 0
	v_mov_b64_e32 v[22:23], 0
	v_mov_b64_e32 v[28:29], 0
	v_mov_b64_e32 v[30:31], 0
	v_mov_b64_e32 v[36:37], 0
	v_mov_b64_e32 v[38:39], 0
	v_mov_b64_e32 v[52:53], 0
	v_mov_b64_e32 v[54:55], 0
	v_mov_b64_e32 v[68:69], 0
	v_mov_b64_e32 v[70:71], 0
	v_mov_b64_e32 v[76:77], 0
	v_mov_b64_e32 v[78:79], 0
	v_mov_b64_e32 v[80:81], 0
	v_mov_b64_e32 v[82:83], 0
	v_mov_b64_e32 v[88:89], 0
	v_mov_b64_e32 v[90:91], 0
	v_mov_b64_e32 v[96:97], 0
	v_mov_b64_e32 v[98:99], 0
	v_mov_b64_e32 v[104:105], 0
	v_mov_b64_e32 v[106:107], 0
	v_mov_b64_e32 v[112:113], 0
	v_mov_b64_e32 v[114:115], 0
	v_mov_b64_e32 v[120:121], 0
	v_mov_b64_e32 v[122:123], 0
	v_mov_b64_e32 v[128:129], 0
	v_mov_b64_e32 v[130:131], 0
	v_mov_b64_e32 v[136:137], 0
	v_mov_b64_e32 v[138:139], 0
	v_mov_b64_e32 v[84:85], 0
	v_mov_b64_e32 v[86:87], 0
	v_mov_b64_e32 v[92:93], 0
	v_mov_b64_e32 v[94:95], 0
	v_mov_b64_e32 v[100:101], 0
	v_mov_b64_e32 v[102:103], 0
	v_mov_b64_e32 v[108:109], 0
	v_mov_b64_e32 v[110:111], 0
	v_mov_b64_e32 v[116:117], 0
	v_mov_b64_e32 v[118:119], 0
	v_mov_b64_e32 v[124:125], 0
	v_mov_b64_e32 v[126:127], 0
	v_mov_b64_e32 v[132:133], 0
	v_mov_b64_e32 v[134:135], 0
	v_mov_b64_e32 v[140:141], 0
	v_mov_b64_e32 v[142:143], 0

.LBB0_332:
	s_and_b32 s25, s16, 3
	v_and_b32_e32 v1, 48, v0
	v_lshlrev_b32_e32 v2, 6, v0
	s_movk_i32 s16, 0x3c0
	v_lshlrev_b32_e32 v0, 2, v0
	s_lshl_b32 s22, s15, 6
	s_lshl_b32 s15, s15, 13
	v_and_or_b32 v1, v2, s16, v1
	v_and_b32_e32 v0, 32, v0
	v_bitop3_b32 v2, v1, s15, v0 bitop3:0xde
	s_lshl_b32 s15, s25, 12
	s_add_u32 s16, s12, 0x80
	v_bitop3_b32 v1, v1, s15, v0 bitop3:0xde
	s_addc_u32 s17, s13, 0
	s_waitcnt vmcnt(0)
	s_barrier
	s_add_i32 m0, s23, 0x18000
	s_mov_b32 s34, -2
	global_load_lds_dwordx4 v36, s[16:17]
	s_add_u32 s16, s12, 0x20080
	s_addc_u32 s17, s13, 0
	s_add_i32 m0, s23, 0x1a000
	v_add_u32_e32 v40, 0, v2
	global_load_lds_dwordx4 v36, s[16:17]
	s_add_u32 s16, s4, 0x80
	s_addc_u32 s17, s5, 0
	s_add_i32 s26, s23, 0x8000
	s_mov_b32 m0, s26
	s_nop 0
	global_load_lds_dwordx4 v37, s[16:17]
	s_add_u32 s16, s4, 0x20080
	s_addc_u32 s17, s5, 0
	s_add_i32 s27, s23, 0xa000
	s_mov_b32 m0, s27
	s_nop 0
	global_load_lds_dwordx4 v37, s[16:17]
	s_add_i32 m0, s23, 0x1c000
	s_add_u32 s16, s12, 0x40080
	s_addc_u32 s17, s13, 0
	s_nop 0
	global_load_lds_dwordx4 v36, s[16:17]
	s_add_u32 s16, s12, 0x60080
	s_addc_u32 s17, s13, 0
	s_add_i32 m0, s23, 0x1e000
	s_add_u32 s28, s12, 0x100
	global_load_lds_dwordx4 v36, s[16:17]
	s_addc_u32 s29, s13, 0
	s_add_u32 s30, s4, 0x100
	s_waitcnt vmcnt(6)
	s_addc_u32 s31, s5, 0
	s_add_i32 s35, 0, 0x10000
	s_add_i32 s37, 0, 0x14000
	s_add_i32 s39, 0, 0x18000
	s_add_i32 s41, 0, 0x1c000
	v_mov_b32_e32 v0, 0
	v_add_u32_e32 v38, s35, v1
	v_add_u32_e32 v39, s37, v1
	s_add_i32 s35, s35, s14
	s_add_i32 s37, s37, s14
	v_add_u32_e32 v41, s39, v1
	v_add_u32_e32 v42, s41, v1
	s_add_i32 s39, s39, s14
	s_add_i32 s41, s41, s14
	s_add_i32 s36, s35, 0x2000
	s_add_i32 s38, s37, 0x2000
	s_add_i32 s40, s39, 0x2000
	s_add_i32 s49, s41, 0x2000
	v_mov_b64_e32 v[0:1], 0
	v_mov_b64_e32 v[2:3], 0
	v_mov_b64_e32 v[8:9], 0
	v_mov_b64_e32 v[10:11], 0
	v_mov_b64_e32 v[16:17], 0
	v_mov_b64_e32 v[18:19], 0
	v_mov_b64_e32 v[24:25], 0
	v_mov_b64_e32 v[26:27], 0
	v_mov_b64_e32 v[32:33], 0
	v_mov_b64_e32 v[34:35], 0
	v_mov_b64_e32 v[48:49], 0
	v_mov_b64_e32 v[50:51], 0
	v_mov_b64_e32 v[64:65], 0
	v_mov_b64_e32 v[66:67], 0
	v_mov_b64_e32 v[72:73], 0
	v_mov_b64_e32 v[74:75], 0
	v_mov_b64_e32 v[4:5], 0
	v_mov_b64_e32 v[6:7], 0
	v_mov_b64_e32 v[12:13], 0
	v_mov_b64_e32 v[14:15], 0
	v_mov_b64_e32 v[20:21], 0
	v_mov_b64_e32 v[22:23], 0
	v_mov_b64_e32 v[28:29], 0
	v_mov_b64_e32 v[30:31], 0
	v_mov_b64_e32 v[44:45], 0
	v_mov_b64_e32 v[46:47], 0
	v_mov_b64_e32 v[60:61], 0
	v_mov_b64_e32 v[62:63], 0
	v_mov_b64_e32 v[68:69], 0
	v_mov_b64_e32 v[70:71], 0
	v_mov_b64_e32 v[76:77], 0
	v_mov_b64_e32 v[78:79], 0
	s_barrier

.LBB0_724:
	s_ashr_i32 s17, s16, 31
	s_lshl_b64 s[18:19], s[16:17], 19
	s_add_u32 s15, s3, s18
	s_addc_u32 s17, s13, s19
	s_and_b64 s[18:19], s[20:21], exec
	s_cselect_b32 s18, s15, s24
	s_cselect_b32 s19, s17, s25
	s_ashr_i32 s15, s14, 31
	s_lshl_b64 s[28:29], s[14:15], 19
	s_add_u32 s15, s34, s28
	s_addc_u32 s17, s35, s29
	s_and_b64 s[20:21], s[20:21], exec
	s_cselect_b32 s20, s15, s26
	s_cselect_b32 s21, s17, s27
	s_add_u32 s15, s26, 0x100
	s_addc_u32 s17, s27, 0
	s_add_u32 s24, s24, 0x60080
	v_mov_b32_e32 v0, 0
	s_addc_u32 s25, s25, 0
	s_mov_b32 s60, -2
	v_mov_b64_e32 v[0:1], 0
	v_mov_b64_e32 v[2:3], 0
	v_mov_b64_e32 v[4:5], 0
	v_mov_b64_e32 v[6:7], 0
	v_mov_b64_e32 v[16:17], 0
	v_mov_b64_e32 v[18:19], 0
	v_mov_b64_e32 v[20:21], 0
	v_mov_b64_e32 v[22:23], 0
	v_mov_b64_e32 v[32:33], 0
	v_mov_b64_e32 v[34:35], 0
	v_mov_b64_e32 v[36:37], 0
	v_mov_b64_e32 v[38:39], 0
	v_mov_b64_e32 v[48:49], 0
	v_mov_b64_e32 v[50:51], 0
	v_mov_b64_e32 v[52:53], 0
	v_mov_b64_e32 v[54:55], 0
	v_mov_b64_e32 v[8:9], 0
	v_mov_b64_e32 v[10:11], 0
	v_mov_b64_e32 v[12:13], 0
	v_mov_b64_e32 v[14:15], 0
	v_mov_b64_e32 v[24:25], 0
	v_mov_b64_e32 v[26:27], 0
	v_mov_b64_e32 v[28:29], 0
	v_mov_b64_e32 v[30:31], 0
	v_mov_b64_e32 v[40:41], 0
	v_mov_b64_e32 v[42:43], 0
	v_mov_b64_e32 v[44:45], 0
	v_mov_b64_e32 v[46:47], 0
	v_mov_b64_e32 v[56:57], 0
	v_mov_b64_e32 v[58:59], 0
	v_mov_b64_e32 v[60:61], 0
	v_mov_b64_e32 v[62:63], 0
	v_mov_b64_e32 v[64:65], 0
	v_mov_b64_e32 v[66:67], 0
	v_mov_b64_e32 v[68:69], 0
	v_mov_b64_e32 v[70:71], 0
	v_mov_b64_e32 v[80:81], 0
	v_mov_b64_e32 v[82:83], 0
	v_mov_b64_e32 v[84:85], 0
	v_mov_b64_e32 v[86:87], 0
	v_mov_b64_e32 v[96:97], 0
	v_mov_b64_e32 v[98:99], 0
	v_mov_b64_e32 v[100:101], 0
	v_mov_b64_e32 v[102:103], 0
	v_mov_b64_e32 v[112:113], 0
	v_mov_b64_e32 v[114:115], 0
	v_mov_b64_e32 v[116:117], 0
	v_mov_b64_e32 v[118:119], 0
	v_mov_b64_e32 v[72:73], 0
	v_mov_b64_e32 v[74:75], 0
	v_mov_b64_e32 v[76:77], 0
	v_mov_b64_e32 v[78:79], 0
	v_mov_b64_e32 v[88:89], 0
	v_mov_b64_e32 v[90:91], 0
	v_mov_b64_e32 v[92:93], 0
	v_mov_b64_e32 v[94:95], 0
	v_mov_b64_e32 v[104:105], 0
	v_mov_b64_e32 v[106:107], 0
	v_mov_b64_e32 v[108:109], 0
	v_mov_b64_e32 v[110:111], 0
	v_mov_b64_e32 v[120:121], 0
	v_mov_b64_e32 v[122:123], 0
	v_mov_b64_e32 v[124:125], 0
	v_mov_b64_e32 v[126:127], 0

.LBB0_1123:
	s_nop 0
	v_readfirstlane_b32 s20, v0
	v_bfe_u32 v0, v128, 16, 16
	s_add_u32 s14, s22, 0x100
	v_lshl_or_b32 v130, v0, 10, v135
	v_bfe_u32 v0, v129, 16, 16
	s_addc_u32 s65, s23, 0
	v_lshl_or_b32 v131, v0, 10, v135
	s_add_u32 s68, s8, 0x100
	v_mov_b32_e32 v0, 0
	v_readfirstlane_b32 s21, v1
	s_addc_u32 s69, s9, 0
	s_mov_b32 s70, -2
	v_mov_b64_e32 v[0:1], 0
	v_mov_b64_e32 v[2:3], 0
	v_mov_b64_e32 v[8:9], 0
	v_mov_b64_e32 v[10:11], 0
	v_mov_b64_e32 v[16:17], 0
	v_mov_b64_e32 v[18:19], 0
	v_mov_b64_e32 v[24:25], 0
	v_mov_b64_e32 v[26:27], 0
	s_waitcnt vmcnt(0)
	v_mov_b64_e32 v[32:33], 0
	v_mov_b64_e32 v[34:35], 0
	v_mov_b64_e32 v[40:41], 0
	v_mov_b64_e32 v[42:43], 0
	v_mov_b64_e32 v[48:49], 0
	v_mov_b64_e32 v[50:51], 0
	v_mov_b64_e32 v[56:57], 0
	v_mov_b64_e32 v[58:59], 0
	v_mov_b64_e32 v[4:5], 0
	v_mov_b64_e32 v[6:7], 0
	v_mov_b64_e32 v[12:13], 0
	v_mov_b64_e32 v[14:15], 0
	v_mov_b64_e32 v[20:21], 0
	v_mov_b64_e32 v[22:23], 0
	v_mov_b64_e32 v[28:29], 0
	v_mov_b64_e32 v[30:31], 0
	v_mov_b64_e32 v[36:37], 0
	v_mov_b64_e32 v[38:39], 0
	v_mov_b64_e32 v[44:45], 0
	v_mov_b64_e32 v[46:47], 0
	v_mov_b64_e32 v[52:53], 0
	v_mov_b64_e32 v[54:55], 0
	v_mov_b64_e32 v[60:61], 0
	v_mov_b64_e32 v[62:63], 0
	v_mov_b64_e32 v[64:65], 0
	v_mov_b64_e32 v[66:67], 0
	v_mov_b64_e32 v[72:73], 0
	v_mov_b64_e32 v[74:75], 0
	v_mov_b64_e32 v[80:81], 0
	v_mov_b64_e32 v[82:83], 0
	v_mov_b64_e32 v[88:89], 0
	v_mov_b64_e32 v[90:91], 0
	v_mov_b64_e32 v[96:97], 0
	v_mov_b64_e32 v[98:99], 0
	v_mov_b64_e32 v[104:105], 0
	v_mov_b64_e32 v[106:107], 0
	v_mov_b64_e32 v[112:113], 0
	v_mov_b64_e32 v[114:115], 0
	v_mov_b64_e32 v[120:121], 0
	v_mov_b64_e32 v[122:123], 0
	v_mov_b64_e32 v[68:69], 0
	v_mov_b64_e32 v[70:71], 0
	v_mov_b64_e32 v[76:77], 0
	v_mov_b64_e32 v[78:79], 0
	v_mov_b64_e32 v[84:85], 0
	v_mov_b64_e32 v[86:87], 0
	v_mov_b64_e32 v[92:93], 0
	v_mov_b64_e32 v[94:95], 0
	v_mov_b64_e32 v[100:101], 0
	v_mov_b64_e32 v[102:103], 0
	v_mov_b64_e32 v[108:109], 0
	v_mov_b64_e32 v[110:111], 0
	v_mov_b64_e32 v[116:117], 0
	v_mov_b64_e32 v[118:119], 0
	v_mov_b64_e32 v[124:125], 0
	v_mov_b64_e32 v[126:127], 0

.LBB0_1285:
	v_and_b32_e32 v0, 48, v6
	v_lshlrev_b32_e32 v1, 6, v6
	s_movk_i32 s5, 0x3c0
	v_and_or_b32 v0, v1, s5, v0
	v_lshlrev_b32_e32 v1, 2, v6
	s_lshl_b32 s4, s17, 13
	v_and_b32_e32 v1, 32, v1
	v_bitop3_b32 v2, v0, s4, v1 bitop3:0xde
	s_lshl_b32 s4, s16, 5
	s_and_b32 s21, s4, 0x60
	s_lshl_b32 s24, s17, 6
	s_lshl_b32 s4, s21, 7
	v_bitop3_b32 v1, s4, v0, v1 bitop3:0xf6
	s_add_u32 s4, s0, 0x80
	s_addc_u32 s5, s1, 0
	s_waitcnt vmcnt(0)
	s_barrier
	s_add_i32 m0, s23, 0x18000
	s_mov_b32 s37, -2
	global_load_lds_dwordx4 v64, s[4:5]
	s_add_u32 s4, s0, 0x10080
	s_addc_u32 s5, s1, 0
	s_add_i32 m0, s23, 0x1a000
	v_add_u32_e32 v69, 0, v2
	global_load_lds_dwordx4 v64, s[4:5]
	s_add_u32 s4, s8, 0x80
	s_addc_u32 s5, s9, 0
	s_add_i32 s26, s23, 0x8000
	s_mov_b64 s[16:17], s[4:5]
	s_mov_b32 m0, s26
	s_add_i32 s27, s23, 0xa000
	s_nop 0
	global_load_lds_dwordx4 v65, s[16:17]
	s_mov_b32 m0, s27
	s_nop 0
	global_load_lds_dwordx4 v66, s[4:5]
	s_add_i32 m0, s23, 0x1c000
	s_add_u32 s4, s0, 0x20080
	s_addc_u32 s5, s1, 0
	s_nop 0
	global_load_lds_dwordx4 v64, s[4:5]
	s_add_u32 s4, s0, 0x30080
	s_addc_u32 s5, s1, 0
	s_add_i32 m0, s23, 0x1e000
	s_add_u32 s31, s0, 0x100
	global_load_lds_dwordx4 v64, s[4:5]
	s_addc_u32 s34, s1, 0
	s_add_u32 s35, s8, 0x100
	s_waitcnt vmcnt(6)
	s_addc_u32 s36, s9, 0
	s_add_i32 s38, 0, 0x10000
	s_add_i32 s40, 0, 0x14000
	s_add_i32 s42, 0, 0x18000
	s_add_i32 s44, 0, 0x1c000
	v_mov_b32_e32 v0, 0
	v_add_u32_e32 v67, s38, v1
	v_add_u32_e32 v68, s40, v1
	s_add_i32 s38, s38, s14
	s_add_i32 s40, s40, s14
	v_add_u32_e32 v70, s42, v1
	v_add_u32_e32 v71, s44, v1
	s_add_i32 s42, s42, s14
	s_add_i32 s44, s44, s14
	s_add_i32 s39, s38, 0x2000
	s_add_i32 s41, s40, 0x2000
	s_add_i32 s43, s42, 0x2000
	s_add_i32 s45, s44, 0x2000
	v_mov_b64_e32 v[0:1], 0
	v_mov_b64_e32 v[2:3], 0
	v_mov_b64_e32 v[8:9], 0
	v_mov_b64_e32 v[10:11], 0
	v_mov_b64_e32 v[16:17], 0
	v_mov_b64_e32 v[18:19], 0
	v_mov_b64_e32 v[24:25], 0
	v_mov_b64_e32 v[26:27], 0
	s_waitcnt vmcnt(0)
	v_mov_b64_e32 v[32:33], 0
	v_mov_b64_e32 v[34:35], 0
	v_mov_b64_e32 v[40:41], 0
	v_mov_b64_e32 v[42:43], 0
	v_mov_b64_e32 v[48:49], 0
	v_mov_b64_e32 v[50:51], 0
	v_mov_b64_e32 v[56:57], 0
	v_mov_b64_e32 v[58:59], 0
	v_mov_b64_e32 v[4:5], 0
	v_mov_b64_e32 v[6:7], 0
	v_mov_b64_e32 v[12:13], 0
	v_mov_b64_e32 v[14:15], 0
	v_mov_b64_e32 v[20:21], 0
	v_mov_b64_e32 v[22:23], 0
	v_mov_b64_e32 v[28:29], 0
	v_mov_b64_e32 v[30:31], 0
	v_mov_b64_e32 v[36:37], 0
	v_mov_b64_e32 v[38:39], 0
	v_mov_b64_e32 v[44:45], 0
	v_mov_b64_e32 v[46:47], 0
	v_mov_b64_e32 v[52:53], 0
	v_mov_b64_e32 v[54:55], 0
	v_mov_b64_e32 v[60:61], 0
	v_mov_b64_e32 v[62:63], 0
	s_barrier

.LBB0_1768:
	s_ashr_i32 s53, s52, 31
	s_lshl_b64 s[60:61], s[52:53], 19
	s_add_u32 s5, s90, s60
	s_addc_u32 s51, s91, s61
	s_and_b64 s[60:61], s[64:65], exec
	s_cselect_b32 s60, s5, s6
	s_cselect_b32 s61, s51, s7
	s_ashr_i32 s51, s50, 31
	s_lshl_b64 s[72:73], s[50:51], 19
	s_add_u32 s5, s3, s72
	s_addc_u32 s51, s21, s73
	s_and_b64 s[64:65], s[64:65], exec
	s_cselect_b32 s64, s5, s70
	s_cselect_b32 s65, s51, s71
	s_add_u32 s5, s70, 0x100
	s_addc_u32 s51, s71, 0
	s_add_u32 s6, s6, 0x60080
	v_mov_b32_e32 v0, 0
	s_addc_u32 s7, s7, 0
	s_mov_b32 s53, -2
	v_mov_b64_e32 v[0:1], 0
	v_mov_b64_e32 v[2:3], 0
	v_mov_b64_e32 v[4:5], 0
	v_mov_b64_e32 v[6:7], 0
	v_mov_b64_e32 v[16:17], 0
	v_mov_b64_e32 v[18:19], 0
	v_mov_b64_e32 v[20:21], 0
	v_mov_b64_e32 v[22:23], 0
	s_waitcnt vmcnt(0)
	v_mov_b64_e32 v[32:33], 0
	v_mov_b64_e32 v[34:35], 0
	v_mov_b64_e32 v[36:37], 0
	v_mov_b64_e32 v[38:39], 0
	v_mov_b64_e32 v[48:49], 0
	v_mov_b64_e32 v[50:51], 0
	v_mov_b64_e32 v[52:53], 0
	v_mov_b64_e32 v[54:55], 0
	v_mov_b64_e32 v[8:9], 0
	v_mov_b64_e32 v[10:11], 0
	v_mov_b64_e32 v[12:13], 0
	v_mov_b64_e32 v[14:15], 0
	v_mov_b64_e32 v[24:25], 0
	v_mov_b64_e32 v[26:27], 0
	v_mov_b64_e32 v[28:29], 0
	v_mov_b64_e32 v[30:31], 0
	v_mov_b64_e32 v[40:41], 0
	v_mov_b64_e32 v[42:43], 0
	v_mov_b64_e32 v[44:45], 0
	v_mov_b64_e32 v[46:47], 0
	v_mov_b64_e32 v[64:65], 0
	v_mov_b64_e32 v[66:67], 0
	v_mov_b64_e32 v[72:73], 0
	v_mov_b64_e32 v[74:75], 0
	v_mov_b64_e32 v[80:81], 0
	v_mov_b64_e32 v[82:83], 0
	v_mov_b64_e32 v[84:85], 0
	v_mov_b64_e32 v[86:87], 0
	v_mov_b64_e32 v[96:97], 0
	v_mov_b64_e32 v[98:99], 0
	v_mov_b64_e32 v[100:101], 0
	v_mov_b64_e32 v[102:103], 0
	v_mov_b64_e32 v[112:113], 0
	v_mov_b64_e32 v[114:115], 0
	v_mov_b64_e32 v[116:117], 0
	v_mov_b64_e32 v[118:119], 0
	v_mov_b64_e32 v[128:129], 0
	v_mov_b64_e32 v[130:131], 0
	v_mov_b64_e32 v[132:133], 0
	v_mov_b64_e32 v[134:135], 0
	v_mov_b64_e32 v[88:89], 0
	v_mov_b64_e32 v[90:91], 0
	v_mov_b64_e32 v[92:93], 0
	v_mov_b64_e32 v[94:95], 0
	v_mov_b64_e32 v[104:105], 0
	v_mov_b64_e32 v[106:107], 0
	v_mov_b64_e32 v[108:109], 0
	v_mov_b64_e32 v[110:111], 0
	v_mov_b64_e32 v[120:121], 0
	v_mov_b64_e32 v[122:123], 0
	v_mov_b64_e32 v[124:125], 0
	v_mov_b64_e32 v[126:127], 0
	v_mov_b64_e32 v[136:137], 0
	v_mov_b64_e32 v[138:139], 0
	v_mov_b64_e32 v[140:141], 0
	v_mov_b64_e32 v[142:143], 0

.LBB0_2136:
	s_ashr_i32 s21, s20, 31
	s_lshl_b64 s[22:23], s[20:21], 19
	s_add_u32 s19, s3, s22
	s_addc_u32 s21, s15, s23
	s_and_b64 s[22:23], s[24:25], exec
	s_cselect_b32 s22, s19, s28
	s_cselect_b32 s23, s21, s29
	s_ashr_i32 s19, s18, 31
	s_lshl_b64 s[34:35], s[18:19], 19
	s_add_u32 s19, s17, s34
	s_addc_u32 s21, s38, s35
	s_and_b64 s[24:25], s[24:25], exec
	s_cselect_b32 s24, s19, s30
	s_cselect_b32 s25, s21, s31
	s_add_u32 s19, s30, 0x100
	s_addc_u32 s21, s31, 0
	s_add_u32 s28, s28, 0x60080
	v_mov_b32_e32 v0, 0
	s_addc_u32 s29, s29, 0
	s_mov_b32 s65, -2
	v_mov_b64_e32 v[0:1], 0
	v_mov_b64_e32 v[2:3], 0
	v_mov_b64_e32 v[4:5], 0
	v_mov_b64_e32 v[6:7], 0
	v_mov_b64_e32 v[24:25], 0
	v_mov_b64_e32 v[26:27], 0
	v_mov_b64_e32 v[28:29], 0
	v_mov_b64_e32 v[30:31], 0
	s_waitcnt vmcnt(0)
	v_mov_b64_e32 v[40:41], 0
	v_mov_b64_e32 v[42:43], 0
	v_mov_b64_e32 v[44:45], 0
	v_mov_b64_e32 v[46:47], 0
	v_mov_b64_e32 v[56:57], 0
	v_mov_b64_e32 v[58:59], 0
	v_mov_b64_e32 v[60:61], 0
	v_mov_b64_e32 v[62:63], 0
	v_mov_b64_e32 v[16:17], 0
	v_mov_b64_e32 v[18:19], 0
	v_mov_b64_e32 v[20:21], 0
	v_mov_b64_e32 v[22:23], 0
	v_mov_b64_e32 v[32:33], 0
	v_mov_b64_e32 v[34:35], 0
	v_mov_b64_e32 v[36:37], 0
	v_mov_b64_e32 v[38:39], 0
	v_mov_b64_e32 v[48:49], 0
	v_mov_b64_e32 v[50:51], 0
	v_mov_b64_e32 v[52:53], 0
	v_mov_b64_e32 v[54:55], 0
	v_mov_b64_e32 v[64:65], 0
	v_mov_b64_e32 v[66:67], 0
	v_mov_b64_e32 v[68:69], 0
	v_mov_b64_e32 v[70:71], 0
	v_mov_b64_e32 v[72:73], 0
	v_mov_b64_e32 v[74:75], 0
	v_mov_b64_e32 v[76:77], 0
	v_mov_b64_e32 v[78:79], 0
	v_mov_b64_e32 v[88:89], 0
	v_mov_b64_e32 v[90:91], 0
	v_mov_b64_e32 v[92:93], 0
	v_mov_b64_e32 v[94:95], 0
	v_mov_b64_e32 v[104:105], 0
	v_mov_b64_e32 v[106:107], 0
	v_mov_b64_e32 v[108:109], 0
	v_mov_b64_e32 v[110:111], 0
	v_mov_b64_e32 v[120:121], 0
	v_mov_b64_e32 v[122:123], 0
	v_mov_b64_e32 v[124:125], 0
	v_mov_b64_e32 v[126:127], 0
	v_mov_b64_e32 v[80:81], 0
	v_mov_b64_e32 v[82:83], 0
	v_mov_b64_e32 v[84:85], 0
	v_mov_b64_e32 v[86:87], 0
	v_mov_b64_e32 v[96:97], 0
	v_mov_b64_e32 v[98:99], 0
	v_mov_b64_e32 v[100:101], 0
	v_mov_b64_e32 v[102:103], 0
	v_mov_b64_e32 v[112:113], 0
	v_mov_b64_e32 v[114:115], 0
	v_mov_b64_e32 v[116:117], 0
	v_mov_b64_e32 v[118:119], 0
	v_mov_b64_e32 v[128:129], 0
	v_mov_b64_e32 v[130:131], 0
	v_mov_b64_e32 v[132:133], 0
	v_mov_b64_e32 v[134:135], 0

.LBB0_2445:
	s_nop 0
	v_readfirstlane_b32 s20, v0
	v_bfe_u32 v0, v128, 16, 16
	s_add_u32 s14, s22, 0x100
	v_lshl_or_b32 v130, v0, 10, v135
	v_bfe_u32 v0, v129, 16, 16
	s_addc_u32 s57, s23, 0
	v_lshl_or_b32 v131, v0, 10, v135
	s_add_u32 s58, s8, 0x100
	v_mov_b32_e32 v0, 0
	v_readfirstlane_b32 s21, v1
	s_addc_u32 s59, s9, 0
	s_mov_b32 s60, -2
	v_mov_b64_e32 v[0:1], 0
	v_mov_b64_e32 v[2:3], 0
	v_mov_b64_e32 v[8:9], 0
	v_mov_b64_e32 v[10:11], 0
	v_mov_b64_e32 v[16:17], 0
	v_mov_b64_e32 v[18:19], 0
	v_mov_b64_e32 v[24:25], 0
	v_mov_b64_e32 v[26:27], 0
	v_mov_b64_e32 v[32:33], 0
	v_mov_b64_e32 v[34:35], 0
	v_mov_b64_e32 v[40:41], 0
	v_mov_b64_e32 v[42:43], 0
	v_mov_b64_e32 v[48:49], 0
	v_mov_b64_e32 v[50:51], 0
	v_mov_b64_e32 v[56:57], 0
	v_mov_b64_e32 v[58:59], 0
	v_mov_b64_e32 v[4:5], 0
	v_mov_b64_e32 v[6:7], 0
	v_mov_b64_e32 v[12:13], 0
	v_mov_b64_e32 v[14:15], 0
	v_mov_b64_e32 v[20:21], 0
	v_mov_b64_e32 v[22:23], 0
	v_mov_b64_e32 v[28:29], 0
	v_mov_b64_e32 v[30:31], 0
	v_mov_b64_e32 v[36:37], 0
	v_mov_b64_e32 v[38:39], 0
	v_mov_b64_e32 v[44:45], 0
	v_mov_b64_e32 v[46:47], 0
	v_mov_b64_e32 v[52:53], 0
	v_mov_b64_e32 v[54:55], 0
	v_mov_b64_e32 v[60:61], 0
	v_mov_b64_e32 v[62:63], 0
	v_mov_b64_e32 v[64:65], 0
	v_mov_b64_e32 v[66:67], 0
	v_mov_b64_e32 v[72:73], 0
	v_mov_b64_e32 v[74:75], 0
	v_mov_b64_e32 v[80:81], 0
	v_mov_b64_e32 v[82:83], 0
	v_mov_b64_e32 v[88:89], 0
	v_mov_b64_e32 v[90:91], 0
	v_mov_b64_e32 v[96:97], 0
	v_mov_b64_e32 v[98:99], 0
	v_mov_b64_e32 v[104:105], 0
	v_mov_b64_e32 v[106:107], 0
	v_mov_b64_e32 v[112:113], 0
	v_mov_b64_e32 v[114:115], 0
	v_mov_b64_e32 v[120:121], 0
	v_mov_b64_e32 v[122:123], 0
	v_mov_b64_e32 v[68:69], 0
	v_mov_b64_e32 v[70:71], 0
	v_mov_b64_e32 v[76:77], 0
	v_mov_b64_e32 v[78:79], 0
	v_mov_b64_e32 v[84:85], 0
	v_mov_b64_e32 v[86:87], 0
	v_mov_b64_e32 v[92:93], 0
	v_mov_b64_e32 v[94:95], 0
	v_mov_b64_e32 v[100:101], 0
	v_mov_b64_e32 v[102:103], 0
	v_mov_b64_e32 v[108:109], 0
	v_mov_b64_e32 v[110:111], 0
	v_mov_b64_e32 v[116:117], 0
	v_mov_b64_e32 v[118:119], 0
	v_mov_b64_e32 v[124:125], 0
	v_mov_b64_e32 v[126:127], 0

.LBB0_2607:
	v_and_b32_e32 v0, 48, v6
	v_lshlrev_b32_e32 v1, 6, v6
	s_movk_i32 s5, 0x3c0
	v_and_or_b32 v0, v1, s5, v0
	v_lshlrev_b32_e32 v1, 2, v6
	s_lshl_b32 s4, s17, 13
	v_and_b32_e32 v1, 32, v1
	v_bitop3_b32 v2, v0, s4, v1 bitop3:0xde
	s_lshl_b32 s4, s16, 5
	s_and_b32 s21, s4, 0x60
	s_lshl_b32 s24, s17, 6
	s_lshl_b32 s4, s21, 7
	v_bitop3_b32 v1, s4, v0, v1 bitop3:0xf6
	s_add_u32 s4, s0, 0x80
	s_addc_u32 s5, s1, 0
	s_waitcnt vmcnt(0)
	s_barrier
	s_add_i32 m0, s23, 0x18000
	s_mov_b32 s36, -2
	global_load_lds_dwordx4 v64, s[4:5]
	s_add_u32 s4, s0, 0x10080
	s_addc_u32 s5, s1, 0
	s_add_i32 m0, s23, 0x1a000
	v_add_u32_e32 v69, 0, v2
	global_load_lds_dwordx4 v64, s[4:5]
	s_add_u32 s4, s8, 0x80
	s_addc_u32 s5, s9, 0
	s_add_i32 s26, s23, 0x8000
	s_mov_b64 s[16:17], s[4:5]
	s_mov_b32 m0, s26
	s_add_i32 s27, s23, 0xa000
	s_nop 0
	global_load_lds_dwordx4 v65, s[16:17]
	s_mov_b32 m0, s27
	s_nop 0
	global_load_lds_dwordx4 v66, s[4:5]
	s_add_i32 m0, s23, 0x1c000
	s_add_u32 s4, s0, 0x20080
	s_addc_u32 s5, s1, 0
	s_nop 0
	global_load_lds_dwordx4 v64, s[4:5]
	s_add_u32 s4, s0, 0x30080
	s_addc_u32 s5, s1, 0
	s_add_i32 m0, s23, 0x1e000
	s_add_u32 s30, s0, 0x100
	global_load_lds_dwordx4 v64, s[4:5]
	s_addc_u32 s31, s1, 0
	s_add_u32 s34, s8, 0x100
	s_waitcnt vmcnt(6)
	s_addc_u32 s35, s9, 0
	s_add_i32 s37, 0, 0x10000
	s_add_i32 s39, 0, 0x14000
	s_add_i32 s41, 0, 0x18000
	s_add_i32 s43, 0, 0x1c000
	v_mov_b32_e32 v0, 0
	v_add_u32_e32 v67, s37, v1
	v_add_u32_e32 v68, s39, v1
	s_add_i32 s37, s37, s14
	s_add_i32 s39, s39, s14
	v_add_u32_e32 v70, s41, v1
	v_add_u32_e32 v71, s43, v1
	s_add_i32 s41, s41, s14
	s_add_i32 s43, s43, s14
	s_add_i32 s38, s37, 0x2000
	s_add_i32 s40, s39, 0x2000
	s_add_i32 s42, s41, 0x2000
	s_add_i32 s44, s43, 0x2000
	v_mov_b64_e32 v[0:1], 0
	v_mov_b64_e32 v[2:3], 0
	v_mov_b64_e32 v[8:9], 0
	v_mov_b64_e32 v[10:11], 0
	v_mov_b64_e32 v[16:17], 0
	v_mov_b64_e32 v[18:19], 0
	v_mov_b64_e32 v[24:25], 0
	v_mov_b64_e32 v[26:27], 0
	v_mov_b64_e32 v[32:33], 0
	v_mov_b64_e32 v[34:35], 0
	v_mov_b64_e32 v[40:41], 0
	v_mov_b64_e32 v[42:43], 0
	v_mov_b64_e32 v[48:49], 0
	v_mov_b64_e32 v[50:51], 0
	v_mov_b64_e32 v[56:57], 0
	v_mov_b64_e32 v[58:59], 0
	v_mov_b64_e32 v[4:5], 0
	v_mov_b64_e32 v[6:7], 0
	v_mov_b64_e32 v[12:13], 0
	v_mov_b64_e32 v[14:15], 0
	v_mov_b64_e32 v[20:21], 0
	v_mov_b64_e32 v[22:23], 0
	v_mov_b64_e32 v[28:29], 0
	v_mov_b64_e32 v[30:31], 0
	v_mov_b64_e32 v[36:37], 0
	v_mov_b64_e32 v[38:39], 0
	v_mov_b64_e32 v[44:45], 0
	v_mov_b64_e32 v[46:47], 0
	v_mov_b64_e32 v[52:53], 0
	v_mov_b64_e32 v[54:55], 0
	v_mov_b64_e32 v[60:61], 0
	v_mov_b64_e32 v[62:63], 0
	s_barrier
